# w1_attn_waits
# speedup vs baseline: 1.0071x; 1.0040x over previous
.LBB1_14:
	v_add_u32_e32 v203, s30, v240
	ds_read_b64_tr_b16 v[196:197], v203 offset:24576
	ds_read_b64_tr_b16 v[198:199], v203 offset:25088
	v_mfma_f32_32x32x16_f16 v[112:127], v[192:195], v[148:151], v[48:63]
	v_cvt_pk_f16_f32 v156, v80, v81
	v_cvt_pk_f16_f32 v157, v82, v83
	ds_read_b64_tr_b16 v[192:193], v203 offset:28672
	ds_read_b64_tr_b16 v[194:195], v203 offset:29184
	v_mfma_f32_32x32x16_f16 v[96:111], v[188:191], v[148:151], v[48:63]
	v_cvt_pk_f16_f32 v158, v84, v85
	v_cvt_pk_f16_f32 v159, v86, v87
	ds_read_b64_tr_b16 v[188:189], v203 offset:25600
	ds_read_b64_tr_b16 v[190:191], v203 offset:26112
	v_mfma_f32_32x32x16_f16 v[112:127], v[184:187], v[140:143], v[112:127]
	v_cvt_pk_f16_f32 v160, v88, v89
	v_cvt_pk_f16_f32 v161, v90, v91
	ds_read_b64_tr_b16 v[88:89], v203 offset:29696
	ds_read_b64_tr_b16 v[90:91], v203 offset:30208
	v_mfma_f32_32x32x16_f16 v[96:111], v[176:179], v[140:143], v[96:111]
	v_cvt_pk_f16_f32 v162, v92, v93
	v_cvt_pk_f16_f32 v163, v94, v95
	ds_read_b64_tr_b16 v[84:85], v203 offset:26624
	ds_read_b64_tr_b16 v[86:87], v203 offset:27136
	v_mfma_f32_32x32x16_f16 v[112:127], v[180:183], v[136:139], v[112:127]
	v_cvt_pk_f16_f32 v152, v64, v65
	v_cvt_pk_f16_f32 v153, v66, v67
	ds_read_b64_tr_b16 v[80:81], v203 offset:30720
	ds_read_b64_tr_b16 v[82:83], v203 offset:31232
	v_mfma_f32_32x32x16_f16 v[96:111], v[172:175], v[136:139], v[96:111]
	v_cvt_pk_f16_f32 v154, v68, v69
	v_cvt_pk_f16_f32 v155, v70, v71
	ds_read_b64_tr_b16 v[68:69], v203 offset:27648
	ds_read_b64_tr_b16 v[70:71], v203 offset:28160
	v_mfma_f32_32x32x16_f16 v[112:127], v[168:171], v[132:135], v[112:127]
	v_cvt_pk_f16_f32 v144, v72, v73
	v_cvt_pk_f16_f32 v145, v74, v75
	ds_read_b64_tr_b16 v[64:65], v203 offset:31744
	ds_read_b64_tr_b16 v[66:67], v203 offset:32256
	v_mfma_f32_32x32x16_f16 v[96:111], v[164:167], v[132:135], v[96:111]
	v_cvt_pk_f16_f32 v146, v76, v77
	v_cvt_pk_f16_f32 v147, v78, v79
	s_add_i32 m0, s48, s38
	s_add_u32 s56, s52, 0x80000
	s_addc_u32 s57, s53, 0
	global_load_lds_dwordx4 v200, s[56:57]
	s_add_i32 m0, m0, 0xfc0
	s_add_u32 s58, s54, 0x40000
	s_addc_u32 s59, s55, 0
	global_load_lds_dwordx4 v200, s[56:57] offset:64
	s_add_i32 m0, s45, s39
	s_nop 0
	global_load_lds_dwordx4 v250, s[58:59]
	s_add_i32 m0, m0, 0xfc0
	s_nop 0
	global_load_lds_dwordx4 v250, s[58:59] offset:64
	v_max_f32_e32 v72, v112, v113
	v_max3_f32 v73, v114, v115, v97
	v_max3_f32 v72, v72, v96, v98
	v_max3_f32 v72, v72, v99, v116
	v_max3_f32 v73, v73, v118, v119
	v_max3_f32 v72, v72, v117, v100
	v_max3_f32 v73, v73, v102, v103
	v_max3_f32 v72, v72, v101, v120
	v_max3_f32 v73, v73, v122, v123
	v_max3_f32 v72, v72, v121, v104
	v_max3_f32 v73, v73, v106, v107
	v_max3_f32 v72, v72, v105, v124
	v_max3_f32 v73, v73, v126, v127
	v_max3_f32 v72, v72, v125, v108
	v_max3_f32 v73, v73, v110, v111
	v_max3_f32 v72, v72, v109, v73
	v_mov_b32_e32 v73, v72
	s_nop 1
	v_permlane32_swap_b32_e32 v72, v73
	v_max_f32_e32 v72, v72, v73
	v_cmp_lt_f32_e32 vcc, s47, v72
	s_cmp_lg_u64 vcc, 0
	s_cselect_b64 s[30:31], -1, 0
	s_cbranch_vccnz .LBB1_22
.LBB1_15:
	s_waitcnt lgkmcnt(0)
	v_mfma_f32_32x32x16_f16 v[0:15], v[156:159], v[196:199], v[0:15]
	v_exp_f32_e32 v112, v112
	v_exp_f32_e32 v113, v113
	v_exp_f32_e32 v114, v114
	v_exp_f32_e32 v115, v115
	v_mfma_f32_32x32x16_f16 v[16:31], v[156:159], v[192:195], v[16:31]
	v_exp_f32_e32 v116, v116
	v_exp_f32_e32 v117, v117
	v_exp_f32_e32 v118, v118
	v_exp_f32_e32 v119, v119
	v_add_u32_e32 v92, s45, v243
	ds_read_b128 v[72:75], v92
	ds_read_b128 v[180:183], v92 offset:512
	v_mfma_f32_32x32x16_f16 v[0:15], v[160:163], v[188:191], v[0:15]
	v_exp_f32_e32 v120, v120
	v_exp_f32_e32 v121, v121
	v_exp_f32_e32 v122, v122
	v_exp_f32_e32 v123, v123
	ds_read_b128 v[184:187], v92 offset:2048
	ds_read_b128 v[168:171], v92 offset:2560
	v_mfma_f32_32x32x16_f16 v[16:31], v[160:163], v[88:91], v[16:31]
	v_exp_f32_e32 v124, v124
	v_exp_f32_e32 v125, v125
	v_exp_f32_e32 v126, v126
	v_exp_f32_e32 v127, v127
	v_pk_add_f16 v76, v156, v160
	v_pk_add_f16 v77, v157, v161
	v_pk_add_f16 v78, v158, v162
	v_pk_add_f16 v79, v159, v163
	v_pk_add_f16 v88, v152, v144
	v_pk_add_f16 v89, v153, v145
	v_pk_add_f16 v90, v154, v146
	v_pk_add_f16 v91, v155, v147
	v_pk_add_f16 v78, v78, v90
	v_pk_add_f16 v79, v79, v91
	v_pk_add_f16 v77, v77, v89
	v_pk_add_f16 v76, v76, v88
	s_nop 1
	v_mfma_f32_32x32x16_f16 v[32:47], v[76:79], v[128:131], v[32:47]
	ds_read_b128 v[188:191], v92 offset:4096
	ds_read_b128 v[172:175], v92 offset:4608
	v_mfma_f32_32x32x16_f16 v[0:15], v[152:155], v[84:87], v[0:15]
	v_exp_f32_e32 v96, v96
	v_exp_f32_e32 v97, v97
	v_exp_f32_e32 v98, v98
	v_exp_f32_e32 v99, v99
	ds_read_b128 v[176:179], v92 offset:6144
	ds_read_b128 v[164:167], v92 offset:6656
	v_mfma_f32_32x32x16_f16 v[16:31], v[152:155], v[80:83], v[16:31]
	v_exp_f32_e32 v100, v100
	v_exp_f32_e32 v101, v101
	v_exp_f32_e32 v102, v102
	v_exp_f32_e32 v103, v103
	v_mfma_f32_32x32x16_f16 v[0:15], v[144:147], v[68:71], v[0:15]
	v_exp_f32_e32 v104, v104
	v_exp_f32_e32 v105, v105
	v_exp_f32_e32 v106, v106
	v_exp_f32_e32 v107, v107
	v_mfma_f32_32x32x16_f16 v[16:31], v[144:147], v[64:67], v[16:31]
	v_exp_f32_e32 v108, v108
	v_exp_f32_e32 v109, v109
	v_exp_f32_e32 v110, v110
	v_exp_f32_e32 v111, v111
	s_waitcnt vmcnt(4) lgkmcnt(0)
	s_barrier
	s_andn2_b64 vcc, exec, s[30:31]
	s_cbranch_vccnz .LBB1_17
	ds_read_b128 v[64:67], v201 offset:49248
	ds_read_b128 v[68:71], v201 offset:49216
	ds_read_b128 v[76:79], v201 offset:49184
	ds_read_b128 v[80:83], v201 offset:49152
	s_waitcnt lgkmcnt(3)
	v_pk_mul_f32 v[12:13], v[12:13], v[64:65]
	s_waitcnt lgkmcnt(2)
	v_pk_mul_f32 v[8:9], v[8:9], v[68:69]
	s_waitcnt lgkmcnt(1)
	v_pk_mul_f32 v[4:5], v[4:5], v[76:77]
	v_pk_mul_f32 v[14:15], v[14:15], v[66:67]
	v_pk_mul_f32 v[10:11], v[10:11], v[70:71]
	v_pk_mul_f32 v[6:7], v[6:7], v[78:79]
	s_waitcnt lgkmcnt(0)
	v_pk_mul_f32 v[2:3], v[2:3], v[82:83]
	v_pk_mul_f32 v[0:1], v[0:1], v[80:81]
	v_pk_mul_f32 v[28:29], v[28:29], v[64:65]
	v_pk_mul_f32 v[24:25], v[24:25], v[68:69]
	v_pk_mul_f32 v[20:21], v[20:21], v[76:77]
	v_pk_mul_f32 v[30:31], v[30:31], v[66:67]
	v_pk_mul_f32 v[26:27], v[26:27], v[70:71]
	v_pk_mul_f32 v[22:23], v[22:23], v[78:79]
	v_pk_mul_f32 v[18:19], v[18:19], v[82:83]
	v_pk_mul_f32 v[16:17], v[16:17], v[80:81]
	v_pk_mul_f32 v[44:45], v[44:45], v[64:65]
	v_pk_mul_f32 v[40:41], v[40:41], v[68:69]
	v_pk_mul_f32 v[36:37], v[36:37], v[76:77]
	v_pk_mul_f32 v[46:47], v[46:47], v[66:67]
	v_pk_mul_f32 v[42:43], v[42:43], v[70:71]
	v_pk_mul_f32 v[38:39], v[38:39], v[78:79]
	v_pk_mul_f32 v[34:35], v[34:35], v[82:83]
	v_pk_mul_f32 v[32:33], v[32:33], v[80:81]
.LBB1_17:
	s_add_i32 s30, s45, 0x2000
	s_cmpk_lg_i32 s45, 0x4000
	s_cselect_b32 s41, s30, 0
	v_add_u32_e32 v203, s48, v240
	ds_read_b64_tr_b16 v[196:197], v203 offset:24576
	ds_read_b64_tr_b16 v[198:199], v203 offset:25088
	v_mfma_f32_32x32x16_f16 v[80:95], v[72:75], v[148:151], v[48:63]
	v_cvt_pk_f16_f32 v156, v112, v113
	v_cvt_pk_f16_f32 v157, v114, v115
	ds_read_b64_tr_b16 v[192:193], v203 offset:28672
	ds_read_b64_tr_b16 v[194:195], v203 offset:29184
	v_mfma_f32_32x32x16_f16 v[64:79], v[180:183], v[148:151], v[48:63]
	v_cvt_pk_f16_f32 v158, v116, v117
	v_cvt_pk_f16_f32 v159, v118, v119
	ds_read_b64_tr_b16 v[180:181], v203 offset:25600
	ds_read_b64_tr_b16 v[182:183], v203 offset:26112
	v_mfma_f32_32x32x16_f16 v[80:95], v[184:187], v[140:143], v[80:95]
	v_cvt_pk_f16_f32 v160, v120, v121
	v_cvt_pk_f16_f32 v161, v122, v123
	ds_read_b64_tr_b16 v[120:121], v203 offset:29696
	ds_read_b64_tr_b16 v[122:123], v203 offset:30208
	v_mfma_f32_32x32x16_f16 v[64:79], v[168:171], v[140:143], v[64:79]
	v_cvt_pk_f16_f32 v162, v124, v125
	v_cvt_pk_f16_f32 v163, v126, v127
	ds_read_b64_tr_b16 v[116:117], v203 offset:26624
	ds_read_b64_tr_b16 v[118:119], v203 offset:27136
	v_mfma_f32_32x32x16_f16 v[80:95], v[188:191], v[136:139], v[80:95]
	v_cvt_pk_f16_f32 v152, v96, v97
	v_cvt_pk_f16_f32 v153, v98, v99
	ds_read_b64_tr_b16 v[112:113], v203 offset:30720
	ds_read_b64_tr_b16 v[114:115], v203 offset:31232
	v_mfma_f32_32x32x16_f16 v[64:79], v[172:175], v[136:139], v[64:79]
	v_cvt_pk_f16_f32 v154, v100, v101
	v_cvt_pk_f16_f32 v155, v102, v103
	ds_read_b64_tr_b16 v[100:101], v203 offset:27648
	ds_read_b64_tr_b16 v[102:103], v203 offset:28160
	v_mfma_f32_32x32x16_f16 v[80:95], v[176:179], v[132:135], v[80:95]
	v_cvt_pk_f16_f32 v144, v104, v105
	v_cvt_pk_f16_f32 v145, v106, v107
	ds_read_b64_tr_b16 v[96:97], v203 offset:31744
	ds_read_b64_tr_b16 v[98:99], v203 offset:32256
	v_mfma_f32_32x32x16_f16 v[64:79], v[164:167], v[132:135], v[64:79]
	v_cvt_pk_f16_f32 v146, v108, v109
	v_cvt_pk_f16_f32 v147, v110, v111
	s_add_i32 m0, s45, s38
	s_add_u32 s56, s52, 0xa0000
	s_addc_u32 s57, s53, 0
	global_load_lds_dwordx4 v200, s[56:57]
	s_add_i32 m0, m0, 0xfc0
	s_add_u32 s58, s54, 0x60000
	s_addc_u32 s59, s55, 0
	global_load_lds_dwordx4 v200, s[56:57] offset:64
	s_add_i32 m0, s41, s39
	s_nop 0
	global_load_lds_dwordx4 v250, s[58:59]
	s_add_i32 m0, m0, 0xfc0
	s_nop 0
	global_load_lds_dwordx4 v250, s[58:59] offset:64
	v_max_f32_e32 v104, v80, v81
	v_max3_f32 v105, v82, v83, v65
	v_max3_f32 v104, v104, v64, v66
	v_max3_f32 v104, v104, v67, v84
	v_max3_f32 v105, v105, v86, v87
	v_max3_f32 v104, v104, v85, v68
	v_max3_f32 v105, v105, v70, v71
	v_max3_f32 v104, v104, v69, v88
	v_max3_f32 v105, v105, v90, v91
	v_max3_f32 v104, v104, v89, v72
	v_max3_f32 v105, v105, v74, v75
	v_max3_f32 v104, v104, v73, v92
	v_max3_f32 v105, v105, v94, v95
	v_max3_f32 v104, v104, v93, v76
	v_max3_f32 v105, v105, v78, v79
	v_max3_f32 v104, v104, v77, v105
	v_mov_b32_e32 v105, v104
	s_nop 1
	v_permlane32_swap_b32_e32 v104, v105
	v_max_f32_e32 v104, v104, v105
	v_cmp_lt_f32_e32 vcc, s47, v104
	s_cmp_lg_u64 vcc, 0
	s_cselect_b64 s[30:31], -1, 0
	s_cbranch_vccnz .LBB1_25
.LBB1_18:
	s_waitcnt lgkmcnt(0)
	v_mfma_f32_32x32x16_f16 v[0:15], v[156:159], v[196:199], v[0:15]
	v_exp_f32_e32 v80, v80
	v_exp_f32_e32 v81, v81
	v_exp_f32_e32 v82, v82
	v_exp_f32_e32 v83, v83
	v_mfma_f32_32x32x16_f16 v[16:31], v[156:159], v[192:195], v[16:31]
	v_exp_f32_e32 v84, v84
	v_exp_f32_e32 v85, v85
	v_exp_f32_e32 v86, v86
	v_exp_f32_e32 v87, v87
	v_add_u32_e32 v108, s41, v243
	ds_read_b128 v[192:195], v108
	ds_read_b128 v[188:191], v108 offset:512
	v_mfma_f32_32x32x16_f16 v[0:15], v[160:163], v[180:183], v[0:15]
	v_exp_f32_e32 v88, v88
	v_exp_f32_e32 v89, v89
	v_exp_f32_e32 v90, v90
	v_exp_f32_e32 v91, v91
	ds_read_b128 v[184:187], v108 offset:2048
	ds_read_b128 v[176:179], v108 offset:2560
	v_mfma_f32_32x32x16_f16 v[16:31], v[160:163], v[120:123], v[16:31]
	v_exp_f32_e32 v92, v92
	v_exp_f32_e32 v93, v93
	v_exp_f32_e32 v94, v94
	v_exp_f32_e32 v95, v95
	v_pk_add_f16 v104, v156, v160
	v_pk_add_f16 v105, v157, v161
	v_pk_add_f16 v106, v158, v162
	v_pk_add_f16 v107, v159, v163
	v_pk_add_f16 v109, v152, v144
	v_pk_add_f16 v110, v153, v145
	v_pk_add_f16 v111, v154, v146
	v_pk_add_f16 v120, v155, v147
	v_pk_add_f16 v106, v106, v111
	v_pk_add_f16 v107, v107, v120
	v_pk_add_f16 v105, v105, v110
	v_pk_add_f16 v104, v104, v109
	s_nop 1
	v_mfma_f32_32x32x16_f16 v[32:47], v[104:107], v[128:131], v[32:47]
	ds_read_b128 v[180:183], v108 offset:4096
	ds_read_b128 v[172:175], v108 offset:4608
	v_mfma_f32_32x32x16_f16 v[0:15], v[152:155], v[116:119], v[0:15]
	v_exp_f32_e32 v64, v64
	v_exp_f32_e32 v65, v65
	v_exp_f32_e32 v66, v66
	v_exp_f32_e32 v67, v67
	ds_read_b128 v[168:171], v108 offset:6144
	ds_read_b128 v[164:167], v108 offset:6656
	v_mfma_f32_32x32x16_f16 v[16:31], v[152:155], v[112:115], v[16:31]
	v_exp_f32_e32 v68, v68
	v_exp_f32_e32 v69, v69
	v_exp_f32_e32 v70, v70
	v_exp_f32_e32 v71, v71
	v_mfma_f32_32x32x16_f16 v[0:15], v[144:147], v[100:103], v[0:15]
	v_exp_f32_e32 v72, v72
	v_exp_f32_e32 v73, v73
	v_exp_f32_e32 v74, v74
	v_exp_f32_e32 v75, v75
	v_mfma_f32_32x32x16_f16 v[16:31], v[144:147], v[96:99], v[16:31]
	v_exp_f32_e32 v76, v76
	v_exp_f32_e32 v77, v77
	v_exp_f32_e32 v78, v78
	v_exp_f32_e32 v79, v79
	s_waitcnt vmcnt(4) lgkmcnt(0)
	s_barrier
	s_andn2_b64 vcc, exec, s[30:31]
	s_cbranch_vccnz .LBB1_20
	ds_read_b128 v[96:99], v201 offset:49248
	ds_read_b128 v[100:103], v201 offset:49216
	ds_read_b128 v[104:107], v201 offset:49184
	ds_read_b128 v[108:111], v201 offset:49152
	s_waitcnt lgkmcnt(3)
	v_pk_mul_f32 v[12:13], v[12:13], v[96:97]
	s_waitcnt lgkmcnt(2)
	v_pk_mul_f32 v[8:9], v[8:9], v[100:101]
	s_waitcnt lgkmcnt(1)
	v_pk_mul_f32 v[4:5], v[4:5], v[104:105]
	v_pk_mul_f32 v[14:15], v[14:15], v[98:99]
	v_pk_mul_f32 v[10:11], v[10:11], v[102:103]
	v_pk_mul_f32 v[6:7], v[6:7], v[106:107]
	s_waitcnt lgkmcnt(0)
	v_pk_mul_f32 v[2:3], v[2:3], v[110:111]
	v_pk_mul_f32 v[0:1], v[0:1], v[108:109]
	v_pk_mul_f32 v[28:29], v[28:29], v[96:97]
	v_pk_mul_f32 v[24:25], v[24:25], v[100:101]
	v_pk_mul_f32 v[20:21], v[20:21], v[104:105]
	v_pk_mul_f32 v[30:31], v[30:31], v[98:99]
	v_pk_mul_f32 v[26:27], v[26:27], v[102:103]
	v_pk_mul_f32 v[22:23], v[22:23], v[106:107]
	v_pk_mul_f32 v[18:19], v[18:19], v[110:111]
	v_pk_mul_f32 v[16:17], v[16:17], v[108:109]
	v_pk_mul_f32 v[44:45], v[44:45], v[96:97]
	v_pk_mul_f32 v[40:41], v[40:41], v[100:101]
	v_pk_mul_f32 v[36:37], v[36:37], v[104:105]
	v_pk_mul_f32 v[46:47], v[46:47], v[98:99]
	v_pk_mul_f32 v[42:43], v[42:43], v[102:103]
	v_pk_mul_f32 v[38:39], v[38:39], v[106:107]
	v_pk_mul_f32 v[34:35], v[34:35], v[110:111]
	v_pk_mul_f32 v[32:33], v[32:33], v[108:109]
